# combo17 + code placement: the four GEMM K-loop heads pinned to a 64-byte boundary (.p2align 6 before the loop label; all four had drifted to 4 mod 8 after the peel)
# speedup vs baseline: 1.0023x; 1.0023x over previous
.LBB0_243:
	s_add_u32 s22, s22, 0x20080
	s_addc_u32 s23, s23, 0
	s_add_u32 s17, s24, 0x100
	v_mov_b32_e32 v183, 0x1200
	s_addc_u32 s19, s25, 0
	s_mov_b32 s28, -2
	ds_read_b128 v[138:141], v134
	ds_read_b128 v[146:149], v134 offset:2048
	ds_read_b128 v[142:145], v135
	ds_read_b128 v[150:153], v135 offset:2048
	ds_read_b128 v[154:157], v134 offset:16384
	ds_read_b128 v[162:165], v134 offset:18432
	ds_read_b128 v[158:161], v135 offset:16384
	ds_read_b128 v[166:169], v135 offset:18432
	s_add_u32 s24, s22, 0xfffe0080
	s_addc_u32 s25, s23, -1
	s_cmp_eq_u32 s28, 4
	s_cselect_b32 s25, s5, s25
	s_cselect_b32 s24, s4, s24
	s_cselect_b32 s27, s21, s19
	s_cselect_b32 s26, s20, s17
	v_mov_b32_e32 v128, v136
	ds_read_b128 v[170:173], v132
	ds_read_b128 v[194:197], v132 offset:2048
	ds_read_b128 v[174:177], v133
	ds_read_b128 v[198:201], v133 offset:2048
	ds_read_b128 v[228:231], v132 offset:4096
	ds_read_b128 v[236:239], v132 offset:6144
	ds_read_b128 v[232:235], v133 offset:4096
	ds_read_b128 v[240:243], v133 offset:6144
	s_add_i32 m0, s30, 0xc000
	s_nop 0
	global_load_lds_dwordx4 v128, s[22:23]
	v_mov_b32_e32 v128, v137
	s_add_i32 m0, s30, 0xe000
	s_nop 0
	global_load_lds_dwordx4 v128, s[22:23]
	s_waitcnt vmcnt(8)
	s_waitcnt lgkmcnt(0)
	s_barrier
	s_setprio 1
	s_waitcnt lgkmcnt(0)
	v_mfma_f32_16x16x128_f8f6f4 v[124:127], v[138:145], v[170:177], 0
	v_mfma_f32_16x16x128_f8f6f4 v[120:123], v[146:153], v[170:177], 0
	v_mfma_f32_16x16x128_f8f6f4 v[108:111], v[138:145], v[194:201], 0
	v_mfma_f32_16x16x128_f8f6f4 v[104:107], v[146:153], v[194:201], 0
	v_mfma_f32_16x16x128_f8f6f4 v[128:131], v[138:145], v[228:235], 0
	v_mfma_f32_16x16x128_f8f6f4 v[178:181], v[146:153], v[228:235], 0
	v_mfma_f32_16x16x128_f8f6f4 v[202:205], v[138:145], v[236:243], 0
	v_mfma_f32_16x16x128_f8f6f4 v[244:247], v[146:153], v[236:243], 0
	s_setprio 0
	s_setprio 1
	v_mfma_f32_16x16x128_f8f6f4 v[116:119], v[154:161], v[170:177], 0
	v_mfma_f32_16x16x128_f8f6f4 v[112:115], v[162:169], v[170:177], 0
	v_mfma_f32_16x16x128_f8f6f4 v[100:103], v[154:161], v[194:201], 0
	v_mfma_f32_16x16x128_f8f6f4 v[96:99], v[162:169], v[194:201], 0
	v_mfma_f32_16x16x128_f8f6f4 v[170:173], v[154:161], v[228:235], 0
	v_mfma_f32_16x16x128_f8f6f4 v[174:177], v[162:169], v[228:235], 0
	v_mfma_f32_16x16x128_f8f6f4 v[194:197], v[154:161], v[236:243], 0
	v_mfma_f32_16x16x128_f8f6f4 v[198:201], v[162:169], v[236:243], 0
	s_setprio 0
	s_barrier
	v_mov_b32_e32 v182, v136
	s_mov_b32 m0, s31
	s_nop 2
	ds_read_b128 v[64:67], v132 offset:16384
	ds_read_b128 v[72:75], v132 offset:18432
	ds_read_b128 v[68:71], v133 offset:16384
	ds_read_b128 v[76:79], v133 offset:18432
	ds_read_b128 v[80:83], v132 offset:20480
	ds_read_b128 v[88:91], v132 offset:22528
	ds_read_b128 v[84:87], v133 offset:20480
	ds_read_b128 v[92:95], v133 offset:22528
	s_add_u32 s64, s26, 0x20000
	global_load_lds_dwordx4 v182, s[26:27]
	v_mov_b32_e32 v182, v137
	s_mov_b32 m0, s33
	s_addc_u32 s65, s27, 0
	global_load_lds_dwordx4 v182, s[26:27]
	v_mov_b32_e32 v182, v136
	s_mov_b32 m0, s34
	s_nop 0
	global_load_lds_dwordx4 v182, s[64:65]
	v_mov_b32_e32 v182, v137
	s_mov_b32 m0, s35
	s_nop 0
	global_load_lds_dwordx4 v182, s[64:65]
	v_mov_b32_e32 v182, v136
	s_mov_b32 m0, s30
	s_nop 0
	global_load_lds_dwordx4 v182, s[24:25]
	v_mov_b32_e32 v182, v137
	s_mov_b32 m0, s36
	s_nop 0
	global_load_lds_dwordx4 v182, s[24:25]
	s_waitcnt vmcnt(8)
	s_waitcnt lgkmcnt(0)
	s_barrier
	s_setprio 1
	s_waitcnt lgkmcnt(0)
	v_mfma_f32_16x16x128_f8f6f4 v[60:63], v[138:145], v[64:71], 0
	v_mfma_f32_16x16x128_f8f6f4 v[56:59], v[146:153], v[64:71], 0
	v_mfma_f32_16x16x128_f8f6f4 v[228:231], v[138:145], v[72:79], 0
	v_mfma_f32_16x16x128_f8f6f4 v[232:235], v[146:153], v[72:79], 0
	v_mfma_f32_16x16x128_f8f6f4 v[236:239], v[138:145], v[80:87], 0
	v_mfma_f32_16x16x128_f8f6f4 v[240:243], v[146:153], v[80:87], 0
	v_mfma_f32_16x16x128_f8f6f4 v[248:251], v[138:145], v[88:95], 0
	v_mfma_f32_16x16x128_f8f6f4 v[186:189], v[146:153], v[88:95], 0
	s_setprio 0
	s_setprio 1
	v_mfma_f32_16x16x128_f8f6f4 v[52:55], v[154:161], v[64:71], 0
	v_mfma_f32_16x16x128_f8f6f4 v[48:51], v[162:169], v[64:71], 0
	v_mfma_f32_16x16x128_f8f6f4 v[190:193], v[154:161], v[72:79], 0
	v_mfma_f32_16x16x128_f8f6f4 v[210:213], v[162:169], v[72:79], 0
	v_mfma_f32_16x16x128_f8f6f4 v[206:209], v[154:161], v[80:87], 0
	v_mfma_f32_16x16x128_f8f6f4 v[214:217], v[162:169], v[80:87], 0
	v_mfma_f32_16x16x128_f8f6f4 v[222:225], v[154:161], v[88:95], 0
	v_mfma_f32_16x16x128_f8f6f4 v[218:221], v[162:169], v[88:95], 0
	s_setprio 0
	s_barrier
	s_nop 4
	ds_read_b128 v[0:3], v134 offset:32768
	ds_read_b128 v[16:19], v134 offset:34816
	ds_read_b128 v[4:7], v135 offset:32768
	ds_read_b128 v[20:23], v135 offset:34816
	ds_read_b128 v[138:141], v134 offset:49152
	ds_read_b128 v[146:149], v134 offset:51200
	ds_read_b128 v[142:145], v135 offset:49152
	ds_read_b128 v[150:153], v135 offset:51200
	s_add_u32 s64, s24, 0x20000
	v_mov_b32_e32 v64, v136
	s_mov_b32 m0, s37
	ds_read_b128 v[8:11], v132 offset:32768
	ds_read_b128 v[24:27], v132 offset:34816
	ds_read_b128 v[12:15], v133 offset:32768
	ds_read_b128 v[28:31], v133 offset:34816
	ds_read_b128 v[32:35], v132 offset:36864
	ds_read_b128 v[40:43], v132 offset:38912
	ds_read_b128 v[36:39], v133 offset:36864
	ds_read_b128 v[44:47], v133 offset:38912
	s_addc_u32 s65, s25, 0
	s_nop 0
	global_load_lds_dwordx4 v64, s[64:65]
	v_mov_b32_e32 v64, v137
	s_mov_b32 m0, s38
	s_nop 0
	global_load_lds_dwordx4 v64, s[64:65]
	s_waitcnt vmcnt(8)
	s_waitcnt lgkmcnt(0)
	s_barrier
	s_setprio 1
	s_waitcnt lgkmcnt(0)
	v_mfma_f32_16x16x128_f8f6f4 v[124:127], v[0:7], v[8:15], v[124:127]
	v_mfma_f32_16x16x128_f8f6f4 v[120:123], v[16:23], v[8:15], v[120:123]
	v_mfma_f32_16x16x128_f8f6f4 v[108:111], v[0:7], v[24:31], v[108:111]
	v_mfma_f32_16x16x128_f8f6f4 v[104:107], v[16:23], v[24:31], v[104:107]
	v_mfma_f32_16x16x128_f8f6f4 v[92:95], v[0:7], v[32:39], v[128:131]
	v_mfma_f32_16x16x128_f8f6f4 v[88:91], v[16:23], v[32:39], v[178:181]
	v_mfma_f32_16x16x128_f8f6f4 v[76:79], v[0:7], v[40:47], v[202:205]
	v_mfma_f32_16x16x128_f8f6f4 v[72:75], v[16:23], v[40:47], v[244:247]
	s_setprio 0
	s_setprio 1
	v_mfma_f32_16x16x128_f8f6f4 v[116:119], v[138:145], v[8:15], v[116:119]
	v_mfma_f32_16x16x128_f8f6f4 v[112:115], v[146:153], v[8:15], v[112:115]
	v_mfma_f32_16x16x128_f8f6f4 v[100:103], v[138:145], v[24:31], v[100:103]
	v_mfma_f32_16x16x128_f8f6f4 v[96:99], v[146:153], v[24:31], v[96:99]
	v_mfma_f32_16x16x128_f8f6f4 v[84:87], v[138:145], v[32:39], v[170:173]
	v_mfma_f32_16x16x128_f8f6f4 v[80:83], v[146:153], v[32:39], v[174:177]
	v_mfma_f32_16x16x128_f8f6f4 v[68:71], v[138:145], v[40:47], v[194:197]
	v_mfma_f32_16x16x128_f8f6f4 v[64:67], v[146:153], v[40:47], v[198:201]
	s_setprio 0
	s_barrier
	v_mov_b32_e32 v184, v136
	ds_read_b128 v[32:35], v132 offset:49152
	ds_read_b128 v[154:157], v132 offset:51200
	ds_read_b128 v[36:39], v133 offset:49152
	ds_read_b128 v[158:161], v133 offset:51200
	ds_read_b128 v[162:165], v132 offset:53248
	ds_read_b128 v[170:173], v132 offset:55296
	ds_read_b128 v[166:169], v133 offset:53248
	ds_read_b128 v[174:177], v133 offset:55296
	s_mov_b32 m0, s42
	v_lshl_add_u64 v[8:9], s[26:27], 0, v[184:185]
	v_lshl_add_u64 v[8:9], v[8:9], 0, s[46:47]
	v_mov_b32_e32 v184, v137
	global_load_lds_dwordx4 v[8:9], off
	s_mov_b32 m0, s43
	v_lshl_add_u64 v[8:9], s[26:27], 0, v[184:185]
	v_lshl_add_u64 v[8:9], v[8:9], 0, s[46:47]
	global_load_lds_dwordx4 v[8:9], off
	s_add_u32 s26, s26, 0x20080
	v_mov_b32_e32 v8, v136
	s_addc_u32 s27, s27, 0
	s_mov_b32 m0, s50
	v_mov_b32_e32 v184, v136
	global_load_lds_dwordx4 v8, s[26:27]
	v_mov_b32_e32 v8, v137
	s_mov_b32 m0, s51
	s_nop 0
	global_load_lds_dwordx4 v8, s[26:27]
	s_mov_b32 m0, s44
	v_lshl_add_u64 v[8:9], s[24:25], 0, v[184:185]
	v_lshl_add_u64 v[8:9], v[8:9], 0, s[46:47]
	v_mov_b32_e32 v184, v137
	global_load_lds_dwordx4 v[8:9], off
	s_mov_b32 m0, s49
	v_lshl_add_u64 v[8:9], s[24:25], 0, v[184:185]
	v_lshl_add_u64 v[8:9], v[8:9], 0, s[46:47]
	global_load_lds_dwordx4 v[8:9], off
	s_waitcnt vmcnt(8)
	s_waitcnt lgkmcnt(0)
	s_barrier
	s_setprio 1
	s_waitcnt lgkmcnt(0)
	v_mfma_f32_16x16x128_f8f6f4 v[60:63], v[0:7], v[32:39], v[60:63]
	v_mfma_f32_16x16x128_f8f6f4 v[56:59], v[16:23], v[32:39], v[56:59]
	v_mfma_f32_16x16x128_f8f6f4 v[44:47], v[0:7], v[154:161], v[228:231]
	v_mfma_f32_16x16x128_f8f6f4 v[40:43], v[16:23], v[154:161], v[232:235]
	v_mfma_f32_16x16x128_f8f6f4 v[28:31], v[0:7], v[162:169], v[236:239]
	v_mfma_f32_16x16x128_f8f6f4 v[24:27], v[16:23], v[162:169], v[240:243]
	v_mfma_f32_16x16x128_f8f6f4 v[12:15], v[0:7], v[170:177], v[248:251]
	v_mfma_f32_16x16x128_f8f6f4 v[8:11], v[16:23], v[170:177], v[186:189]
	s_setprio 0
	s_setprio 1
	v_mfma_f32_16x16x128_f8f6f4 v[52:55], v[138:145], v[32:39], v[52:55]
	v_mfma_f32_16x16x128_f8f6f4 v[48:51], v[146:153], v[32:39], v[48:51]
	v_mfma_f32_16x16x128_f8f6f4 v[36:39], v[138:145], v[154:161], v[190:193]
	v_mfma_f32_16x16x128_f8f6f4 v[32:35], v[146:153], v[154:161], v[210:213]
	v_mfma_f32_16x16x128_f8f6f4 v[20:23], v[138:145], v[162:169], v[206:209]
	v_mfma_f32_16x16x128_f8f6f4 v[16:19], v[146:153], v[162:169], v[214:217]
	v_mfma_f32_16x16x128_f8f6f4 v[4:7], v[138:145], v[170:177], v[222:225]
	v_mfma_f32_16x16x128_f8f6f4 v[0:3], v[146:153], v[170:177], v[218:221]
	s_setprio 0
	s_barrier
	s_add_i32 s28, s28, 2
	s_add_u32 s22, s22, 0x100
	s_addc_u32 s23, s23, 0
	s_add_u32 s17, s17, 0x100
	s_addc_u32 s19, s19, 0
	.p2align	6

.LBB0_750:
	s_ashr_i32 s19, s18, 31
	s_lshl_b64 s[20:21], s[18:19], 18
	s_add_u32 s20, s33, s20
	s_addc_u32 s21, s34, s21
	s_and_b64 s[22:23], s[2:3], exec
	s_cselect_b32 s5, s21, s27
	s_cselect_b32 s19, s20, s26
	s_ashr_i32 s17, s16, 31
	s_lshl_b64 s[22:23], s[16:17], 18
	s_add_u32 s22, s35, s22
	s_addc_u32 s23, s36, s23
	s_and_b64 s[30:31], s[2:3], exec
	s_cselect_b32 s17, s23, s29
	s_cselect_b32 s25, s22, s28
	s_add_u32 s26, s26, 0x20080
	s_addc_u32 s27, s27, 0
	s_add_u32 s68, s28, 0x100
	v_mov_b32_e32 v183, 0x1200
	s_addc_u32 s70, s29, 0
	s_mov_b32 s72, -2
	ds_read_b128 v[128:131], v162
	ds_read_b128 v[136:139], v162 offset:2048
	ds_read_b128 v[132:135], v163
	ds_read_b128 v[140:143], v163 offset:2048
	ds_read_b128 v[144:147], v162 offset:16384
	ds_read_b128 v[152:155], v162 offset:18432
	ds_read_b128 v[148:151], v163 offset:16384
	ds_read_b128 v[156:159], v163 offset:18432
	s_add_u32 s28, s26, 0xfffe0080
	s_addc_u32 s29, s27, -1
	s_cmp_eq_u32 s72, 4
	s_cselect_b32 s29, s5, s29
	s_cselect_b32 s28, s19, s28
	s_cselect_b32 s31, s17, s70
	s_cselect_b32 s30, s25, s68
	v_mov_b32_e32 v182, v164
	ds_read_b128 v[166:169], v160
	ds_read_b128 v[174:177], v160 offset:2048
	ds_read_b128 v[170:173], v161
	ds_read_b128 v[178:181], v161 offset:2048
	ds_read_b128 v[194:197], v160 offset:4096
	ds_read_b128 v[228:231], v160 offset:6144
	ds_read_b128 v[198:201], v161 offset:4096
	ds_read_b128 v[232:235], v161 offset:6144
	s_add_i32 m0, s37, 0xc000
	s_nop 0
	global_load_lds_dwordx4 v182, s[26:27]
	v_mov_b32_e32 v182, v165
	s_add_i32 m0, s37, 0xe000
	s_nop 0
	global_load_lds_dwordx4 v182, s[26:27]
	s_waitcnt vmcnt(8)
	s_waitcnt lgkmcnt(0)
	s_barrier
	s_setprio 1
	s_waitcnt lgkmcnt(0)
	v_mfma_f32_16x16x128_f8f6f4 v[124:127], v[128:135], v[166:173], 0
	v_mfma_f32_16x16x128_f8f6f4 v[120:123], v[136:143], v[166:173], 0
	v_mfma_f32_16x16x128_f8f6f4 v[108:111], v[128:135], v[174:181], 0
	v_mfma_f32_16x16x128_f8f6f4 v[104:107], v[136:143], v[174:181], 0
	v_mfma_f32_16x16x128_f8f6f4 v[186:189], v[128:135], v[194:201], 0
	v_mfma_f32_16x16x128_f8f6f4 v[190:193], v[136:143], v[194:201], 0
	v_mfma_f32_16x16x128_f8f6f4 v[202:205], v[128:135], v[228:235], 0
	v_mfma_f32_16x16x128_f8f6f4 v[206:209], v[136:143], v[228:235], 0
	s_setprio 0
	s_setprio 1
	v_mfma_f32_16x16x128_f8f6f4 v[116:119], v[144:151], v[166:173], 0
	v_mfma_f32_16x16x128_f8f6f4 v[112:115], v[152:159], v[166:173], 0
	v_mfma_f32_16x16x128_f8f6f4 v[100:103], v[144:151], v[174:181], 0
	v_mfma_f32_16x16x128_f8f6f4 v[96:99], v[152:159], v[174:181], 0
	v_mfma_f32_16x16x128_f8f6f4 v[166:169], v[144:151], v[194:201], 0
	v_mfma_f32_16x16x128_f8f6f4 v[170:173], v[152:159], v[194:201], 0
	v_mfma_f32_16x16x128_f8f6f4 v[174:177], v[144:151], v[228:235], 0
	v_mfma_f32_16x16x128_f8f6f4 v[178:181], v[152:159], v[228:235], 0
	s_setprio 0
	s_barrier
	v_mov_b32_e32 v182, v164
	s_mov_b32 m0, s38
	s_nop 2
	ds_read_b128 v[64:67], v160 offset:16384
	ds_read_b128 v[72:75], v160 offset:18432
	ds_read_b128 v[68:71], v161 offset:16384
	ds_read_b128 v[76:79], v161 offset:18432
	ds_read_b128 v[80:83], v160 offset:20480
	ds_read_b128 v[88:91], v160 offset:22528
	ds_read_b128 v[84:87], v161 offset:20480
	ds_read_b128 v[92:95], v161 offset:22528
	s_add_u32 s74, s30, 0x20000
	global_load_lds_dwordx4 v182, s[30:31]
	v_mov_b32_e32 v182, v165
	s_mov_b32 m0, s39
	s_addc_u32 s75, s31, 0
	global_load_lds_dwordx4 v182, s[30:31]
	v_mov_b32_e32 v182, v164
	s_mov_b32 m0, s40
	s_nop 0
	global_load_lds_dwordx4 v182, s[74:75]
	v_mov_b32_e32 v182, v165
	s_mov_b32 m0, s42
	s_nop 0
	global_load_lds_dwordx4 v182, s[74:75]
	v_mov_b32_e32 v182, v164
	s_mov_b32 m0, s37
	s_nop 0
	global_load_lds_dwordx4 v182, s[28:29]
	v_mov_b32_e32 v182, v165
	s_mov_b32 m0, s43
	s_nop 0
	global_load_lds_dwordx4 v182, s[28:29]
	s_waitcnt vmcnt(8)
	s_waitcnt lgkmcnt(0)
	s_barrier
	s_setprio 1
	s_waitcnt lgkmcnt(0)
	v_mfma_f32_16x16x128_f8f6f4 v[60:63], v[128:135], v[64:71], 0
	v_mfma_f32_16x16x128_f8f6f4 v[56:59], v[136:143], v[64:71], 0
	v_mfma_f32_16x16x128_f8f6f4 v[194:197], v[128:135], v[72:79], 0
	v_mfma_f32_16x16x128_f8f6f4 v[198:201], v[136:143], v[72:79], 0
	v_mfma_f32_16x16x128_f8f6f4 v[210:213], v[128:135], v[80:87], 0
	v_mfma_f32_16x16x128_f8f6f4 v[214:217], v[136:143], v[80:87], 0
	v_mfma_f32_16x16x128_f8f6f4 v[218:221], v[128:135], v[88:95], 0
	v_mfma_f32_16x16x128_f8f6f4 v[222:225], v[136:143], v[88:95], 0
	s_setprio 0
	s_setprio 1
	v_mfma_f32_16x16x128_f8f6f4 v[52:55], v[144:151], v[64:71], 0
	v_mfma_f32_16x16x128_f8f6f4 v[48:51], v[152:159], v[64:71], 0
	v_mfma_f32_16x16x128_f8f6f4 v[228:231], v[144:151], v[72:79], 0
	v_mfma_f32_16x16x128_f8f6f4 v[232:235], v[152:159], v[72:79], 0
	v_mfma_f32_16x16x128_f8f6f4 v[236:239], v[144:151], v[80:87], 0
	v_mfma_f32_16x16x128_f8f6f4 v[240:243], v[152:159], v[80:87], 0
	v_mfma_f32_16x16x128_f8f6f4 v[244:247], v[144:151], v[88:95], 0
	v_mfma_f32_16x16x128_f8f6f4 v[248:251], v[152:159], v[88:95], 0
	s_setprio 0
	s_barrier
	s_nop 4
	ds_read_b128 v[0:3], v162 offset:32768
	ds_read_b128 v[16:19], v162 offset:34816
	ds_read_b128 v[4:7], v163 offset:32768
	ds_read_b128 v[20:23], v163 offset:34816
	ds_read_b128 v[128:131], v162 offset:49152
	ds_read_b128 v[136:139], v162 offset:51200
	ds_read_b128 v[132:135], v163 offset:49152
	ds_read_b128 v[140:143], v163 offset:51200
	s_add_u32 s74, s28, 0x20000
	v_mov_b32_e32 v64, v164
	s_mov_b32 m0, s44
	ds_read_b128 v[8:11], v160 offset:32768
	ds_read_b128 v[24:27], v160 offset:34816
	ds_read_b128 v[12:15], v161 offset:32768
	ds_read_b128 v[28:31], v161 offset:34816
	ds_read_b128 v[32:35], v160 offset:36864
	ds_read_b128 v[40:43], v160 offset:38912
	ds_read_b128 v[36:39], v161 offset:36864
	ds_read_b128 v[44:47], v161 offset:38912
	s_addc_u32 s75, s29, 0
	s_nop 0
	global_load_lds_dwordx4 v64, s[74:75]
	v_mov_b32_e32 v64, v165
	s_mov_b32 m0, s49
	s_nop 0
	global_load_lds_dwordx4 v64, s[74:75]
	s_waitcnt vmcnt(8)
	s_waitcnt lgkmcnt(0)
	s_barrier
	s_setprio 1
	s_waitcnt lgkmcnt(0)
	v_mfma_f32_16x16x128_f8f6f4 v[124:127], v[0:7], v[8:15], v[124:127]
	v_mfma_f32_16x16x128_f8f6f4 v[120:123], v[16:23], v[8:15], v[120:123]
	v_mfma_f32_16x16x128_f8f6f4 v[108:111], v[0:7], v[24:31], v[108:111]
	v_mfma_f32_16x16x128_f8f6f4 v[104:107], v[16:23], v[24:31], v[104:107]
	v_mfma_f32_16x16x128_f8f6f4 v[92:95], v[0:7], v[32:39], v[186:189]
	v_mfma_f32_16x16x128_f8f6f4 v[88:91], v[16:23], v[32:39], v[190:193]
	v_mfma_f32_16x16x128_f8f6f4 v[76:79], v[0:7], v[40:47], v[202:205]
	v_mfma_f32_16x16x128_f8f6f4 v[72:75], v[16:23], v[40:47], v[206:209]
	s_setprio 0
	s_setprio 1
	v_mfma_f32_16x16x128_f8f6f4 v[116:119], v[128:135], v[8:15], v[116:119]
	v_mfma_f32_16x16x128_f8f6f4 v[112:115], v[136:143], v[8:15], v[112:115]
	v_mfma_f32_16x16x128_f8f6f4 v[100:103], v[128:135], v[24:31], v[100:103]
	v_mfma_f32_16x16x128_f8f6f4 v[96:99], v[136:143], v[24:31], v[96:99]
	v_mfma_f32_16x16x128_f8f6f4 v[84:87], v[128:135], v[32:39], v[166:169]
	v_mfma_f32_16x16x128_f8f6f4 v[80:83], v[136:143], v[32:39], v[170:173]
	v_mfma_f32_16x16x128_f8f6f4 v[68:71], v[128:135], v[40:47], v[174:177]
	v_mfma_f32_16x16x128_f8f6f4 v[64:67], v[136:143], v[40:47], v[178:181]
	s_setprio 0
	s_barrier
	v_mov_b32_e32 v184, v164
	ds_read_b128 v[32:35], v160 offset:49152
	ds_read_b128 v[144:147], v160 offset:51200
	ds_read_b128 v[36:39], v161 offset:49152
	ds_read_b128 v[148:151], v161 offset:51200
	ds_read_b128 v[152:155], v160 offset:53248
	ds_read_b128 v[166:169], v160 offset:55296
	ds_read_b128 v[156:159], v161 offset:53248
	ds_read_b128 v[170:173], v161 offset:55296
	s_mov_b32 m0, s54
	v_lshl_add_u64 v[8:9], s[30:31], 0, v[184:185]
	v_lshl_add_u64 v[8:9], v[8:9], 0, s[46:47]
	v_mov_b32_e32 v184, v165
	global_load_lds_dwordx4 v[8:9], off
	s_mov_b32 m0, s55
	v_lshl_add_u64 v[8:9], s[30:31], 0, v[184:185]
	v_lshl_add_u64 v[8:9], v[8:9], 0, s[46:47]
	global_load_lds_dwordx4 v[8:9], off
	s_add_u32 s30, s30, 0x20080
	v_mov_b32_e32 v8, v164
	s_addc_u32 s31, s31, 0
	s_mov_b32 m0, s59
	v_mov_b32_e32 v184, v164
	global_load_lds_dwordx4 v8, s[30:31]
	v_mov_b32_e32 v8, v165
	s_mov_b32 m0, s64
	s_nop 0
	global_load_lds_dwordx4 v8, s[30:31]
	s_mov_b32 m0, s56
	v_lshl_add_u64 v[8:9], s[28:29], 0, v[184:185]
	v_lshl_add_u64 v[8:9], v[8:9], 0, s[46:47]
	v_mov_b32_e32 v184, v165
	global_load_lds_dwordx4 v[8:9], off
	s_mov_b32 m0, s57
	v_lshl_add_u64 v[8:9], s[28:29], 0, v[184:185]
	v_lshl_add_u64 v[8:9], v[8:9], 0, s[46:47]
	global_load_lds_dwordx4 v[8:9], off
	s_waitcnt vmcnt(8)
	s_waitcnt lgkmcnt(0)
	s_barrier
	s_setprio 1
	s_waitcnt lgkmcnt(0)
	v_mfma_f32_16x16x128_f8f6f4 v[60:63], v[0:7], v[32:39], v[60:63]
	v_mfma_f32_16x16x128_f8f6f4 v[56:59], v[16:23], v[32:39], v[56:59]
	v_mfma_f32_16x16x128_f8f6f4 v[44:47], v[0:7], v[144:151], v[194:197]
	v_mfma_f32_16x16x128_f8f6f4 v[40:43], v[16:23], v[144:151], v[198:201]
	v_mfma_f32_16x16x128_f8f6f4 v[28:31], v[0:7], v[152:159], v[210:213]
	v_mfma_f32_16x16x128_f8f6f4 v[24:27], v[16:23], v[152:159], v[214:217]
	v_mfma_f32_16x16x128_f8f6f4 v[12:15], v[0:7], v[166:173], v[218:221]
	v_mfma_f32_16x16x128_f8f6f4 v[8:11], v[16:23], v[166:173], v[222:225]
	s_setprio 0
	s_setprio 1
	v_mfma_f32_16x16x128_f8f6f4 v[52:55], v[128:135], v[32:39], v[52:55]
	v_mfma_f32_16x16x128_f8f6f4 v[48:51], v[136:143], v[32:39], v[48:51]
	v_mfma_f32_16x16x128_f8f6f4 v[36:39], v[128:135], v[144:151], v[228:231]
	v_mfma_f32_16x16x128_f8f6f4 v[32:35], v[136:143], v[144:151], v[232:235]
	v_mfma_f32_16x16x128_f8f6f4 v[20:23], v[128:135], v[152:159], v[236:239]
	v_mfma_f32_16x16x128_f8f6f4 v[16:19], v[136:143], v[152:159], v[240:243]
	v_mfma_f32_16x16x128_f8f6f4 v[4:7], v[128:135], v[166:173], v[244:247]
	v_mfma_f32_16x16x128_f8f6f4 v[0:3], v[136:143], v[166:173], v[248:251]
	s_setprio 0
	s_barrier
	s_add_i32 s72, s72, 2
	s_add_u32 s26, s26, 0x100
	s_addc_u32 s27, s27, 0
	s_add_u32 s68, s68, 0x100
	s_addc_u32 s70, s70, 0
	.p2align	6

.LBB0_1034:
	v_readfirstlane_b32 s19, v4
	s_xor_b32 s27, s75, s19
	s_lshl_b32 s19, s75, 12
	s_add_i32 s74, s19, 0
	s_add_i32 s74, s74, 0x21000
	s_add_u32 s19, s24, 0x100
	s_addc_u32 s76, s25, 0
	s_mov_b32 s77, -2
	s_mov_b64 s[24:25], s[14:15]
	ds_read_b128 v[136:139], v150
	s_waitcnt vmcnt(0)
	ds_read_b128 v[156:159], v150 offset:2048
	ds_read_b128 v[140:143], v151
	ds_read_b128 v[160:163], v151 offset:2048
	ds_read_b128 v[164:167], v150 offset:16384
	ds_read_b128 v[172:175], v150 offset:18432
	ds_read_b128 v[168:171], v151 offset:16384
	ds_read_b128 v[176:179], v151 offset:18432
	s_add_u32 s28, s24, 0x80
	s_addc_u32 s29, s25, 0
	s_cmp_eq_u32 s77, 4
	s_cselect_b32 s29, s11, s29
	s_cselect_b32 s28, s10, s28
	s_cselect_b32 s80, s27, s75
	s_cselect_b32 s37, s23, s76
	s_cselect_b32 s36, s22, s19
	ds_read_b128 v[194:197], v148
	ds_read_b128 v[228:231], v148 offset:2048
	ds_read_b128 v[198:201], v149
	ds_read_b128 v[232:235], v149 offset:2048
	ds_read_b128 v[236:239], v148 offset:4096
	ds_read_b128 v[244:247], v148 offset:6144
	ds_read_b128 v[240:243], v149 offset:4096
	ds_read_b128 v[248:251], v149 offset:6144
	v_mbcnt_lo_u32_b32 v40, -1, 0
	v_mbcnt_hi_u32_b32 v40, -1, v40
	s_mov_b32 s78, s61
	v_lshlrev_b32_e32 v40, 3, v40
	s_add_i32 m0, s35, 0xc000
	v_lshl_or_b32 v40, s78, 9, v40
	v_add_u32_e32 v40, s74, v40
	ds_read_b32 v40, v40 offset:4
	s_waitcnt lgkmcnt(0)
	v_lshlrev_b32_e32 v41, 10, v40
	v_and_or_b32 v41, v41, s69, v154
	v_bfe_u32 v40, v40, 16, 16
	v_lshl_or_b32 v40, v40, 10, v154
	global_load_lds_dwordx4 v41, s[24:25]
	s_add_i32 m0, s35, 0xe000
	s_nop 0
	global_load_lds_dwordx4 v40, s[24:25]
	s_waitcnt vmcnt(8)
	s_waitcnt lgkmcnt(0)
	s_barrier
	s_setprio 1
	v_mfma_f32_16x16x128_f8f6f4 v[132:135], v[136:143], v[194:201], 0
	v_mfma_f32_16x16x128_f8f6f4 v[124:127], v[156:163], v[194:201], 0
	v_mfma_f32_16x16x128_f8f6f4 v[116:119], v[136:143], v[228:235], 0
	v_mfma_f32_16x16x128_f8f6f4 v[108:111], v[156:163], v[228:235], 0
	v_mfma_f32_16x16x128_f8f6f4 v[144:147], v[136:143], v[236:243], 0
	v_mfma_f32_16x16x128_f8f6f4 v[180:183], v[156:163], v[236:243], 0
	v_mfma_f32_16x16x128_f8f6f4 v[186:189], v[136:143], v[244:251], 0
	v_mfma_f32_16x16x128_f8f6f4 v[190:193], v[156:163], v[244:251], 0
	s_setprio 0
	s_setprio 1
	v_mfma_f32_16x16x128_f8f6f4 v[128:131], v[164:171], v[194:201], 0
	v_mfma_f32_16x16x128_f8f6f4 v[120:123], v[172:179], v[194:201], 0
	v_mfma_f32_16x16x128_f8f6f4 v[112:115], v[164:171], v[228:235], 0
	v_mfma_f32_16x16x128_f8f6f4 v[104:107], v[172:179], v[228:235], 0
	v_mfma_f32_16x16x128_f8f6f4 v[202:205], v[164:171], v[236:243], 0
	v_mfma_f32_16x16x128_f8f6f4 v[206:209], v[172:179], v[236:243], 0
	v_mfma_f32_16x16x128_f8f6f4 v[210:213], v[164:171], v[244:251], 0
	v_mfma_f32_16x16x128_f8f6f4 v[214:217], v[172:179], v[244:251], 0
	s_setprio 0
	s_barrier
	v_mov_b32_e32 v40, v152
	s_mov_b32 m0, s44
	s_nop 2
	ds_read_b128 v[72:75], v148 offset:16384
	ds_read_b128 v[80:83], v148 offset:18432
	ds_read_b128 v[76:79], v149 offset:16384
	ds_read_b128 v[84:87], v149 offset:18432
	ds_read_b128 v[88:91], v148 offset:20480
	ds_read_b128 v[96:99], v148 offset:22528
	ds_read_b128 v[92:95], v149 offset:20480
	ds_read_b128 v[100:103], v149 offset:22528
	s_add_u32 s78, s36, 0x20000
	global_load_lds_dwordx4 v40, s[36:37]
	v_mov_b32_e32 v40, v153
	s_mov_b32 m0, s49
	s_addc_u32 s79, s37, 0
	global_load_lds_dwordx4 v40, s[36:37]
	v_mov_b32_e32 v40, v152
	s_mov_b32 m0, s50
	s_nop 0
	global_load_lds_dwordx4 v40, s[78:79]
	v_mov_b32_e32 v40, v153
	s_mov_b32 m0, s51
	s_nop 0
	global_load_lds_dwordx4 v40, s[78:79]
	v_mbcnt_lo_u32_b32 v40, -1, 0
	v_mbcnt_hi_u32_b32 v40, -1, v40
	s_mov_b32 s78, s61
	v_lshlrev_b32_e32 v40, 3, v40
	v_lshl_or_b32 v40, s78, 9, v40
	s_lshl_b32 s78, s80, 12
	s_add_i32 s78, s78, 0
	s_add_i32 s78, s78, 0x21000
	v_add_u32_e32 v40, s78, v40
	ds_read_b32 v40, v40
	s_mov_b32 m0, s35
	s_waitcnt lgkmcnt(0)
	v_lshlrev_b32_e32 v41, 10, v40
	v_and_or_b32 v41, v41, s69, v154
	v_bfe_u32 v40, v40, 16, 16
	v_lshl_or_b32 v40, v40, 10, v154
	global_load_lds_dwordx4 v41, s[28:29]
	s_mov_b32 m0, s54
	s_nop 0
	global_load_lds_dwordx4 v40, s[28:29]
	s_waitcnt vmcnt(8)
	s_waitcnt lgkmcnt(0)
	s_barrier
	s_setprio 1
	v_mfma_f32_16x16x128_f8f6f4 v[48:51], v[136:143], v[80:87], 0
	v_mfma_f32_16x16x128_f8f6f4 v[36:39], v[156:163], v[80:87], 0
	v_mfma_f32_16x16x128_f8f6f4 v[28:31], v[136:143], v[88:95], 0
	v_mfma_f32_16x16x128_f8f6f4 v[20:23], v[156:163], v[88:95], 0
	v_mfma_f32_16x16x128_f8f6f4 v[12:15], v[136:143], v[96:103], 0
	v_mfma_f32_16x16x128_f8f6f4 v[4:7], v[156:163], v[96:103], 0
	v_mfma_f32_16x16x128_f8f6f4 v[40:43], v[136:143], v[72:79], 0
	v_mfma_f32_16x16x128_f8f6f4 v[52:55], v[156:163], v[72:79], 0
	s_setprio 0
	s_setprio 1
	v_mfma_f32_16x16x128_f8f6f4 v[64:67], v[164:171], v[72:79], 0
	v_mfma_f32_16x16x128_f8f6f4 v[56:59], v[172:179], v[72:79], 0
	v_mfma_f32_16x16x128_f8f6f4 v[44:47], v[164:171], v[80:87], 0
	v_mfma_f32_16x16x128_f8f6f4 v[32:35], v[172:179], v[80:87], 0
	v_mfma_f32_16x16x128_f8f6f4 v[24:27], v[164:171], v[88:95], 0
	v_mfma_f32_16x16x128_f8f6f4 v[16:19], v[172:179], v[88:95], 0
	v_mfma_f32_16x16x128_f8f6f4 v[8:11], v[164:171], v[96:103], 0
	v_mfma_f32_16x16x128_f8f6f4 v[0:3], v[172:179], v[96:103], 0
	s_setprio 0
	s_barrier
	ds_read_b128 v[136:139], v150 offset:32768
	ds_read_b128 v[156:159], v150 offset:34816
	ds_read_b128 v[140:143], v151 offset:32768
	ds_read_b128 v[160:163], v151 offset:34816
	ds_read_b128 v[164:167], v150 offset:49152
	ds_read_b128 v[172:175], v150 offset:51200
	ds_read_b128 v[168:171], v151 offset:49152
	ds_read_b128 v[176:179], v151 offset:51200
	ds_read_b128 v[68:71], v148 offset:32768
	ds_read_b128 v[194:197], v148 offset:34816
	ds_read_b128 v[72:75], v149 offset:32768
	ds_read_b128 v[198:201], v149 offset:34816
	ds_read_b128 v[228:231], v148 offset:36864
	ds_read_b128 v[236:239], v148 offset:38912
	ds_read_b128 v[232:235], v149 offset:36864
	ds_read_b128 v[240:243], v149 offset:38912
	v_mbcnt_lo_u32_b32 v60, -1, 0
	v_mbcnt_hi_u32_b32 v60, -1, v60
	s_mov_b32 s79, s61
	v_lshlrev_b32_e32 v60, 3, v60
	s_mov_b32 m0, s55
	v_lshl_or_b32 v60, s79, 9, v60
	v_add_u32_e32 v60, s78, v60
	ds_read_b32 v60, v60 offset:4
	s_waitcnt lgkmcnt(0)
	v_lshlrev_b32_e32 v61, 10, v60
	v_and_or_b32 v61, v61, s69, v154
	v_bfe_u32 v60, v60, 16, 16
	v_lshl_or_b32 v60, v60, 10, v154
	global_load_lds_dwordx4 v61, s[28:29]
	s_mov_b32 m0, s56
	s_nop 0
	global_load_lds_dwordx4 v60, s[28:29]
	s_waitcnt vmcnt(8)
	s_waitcnt lgkmcnt(0)
	s_barrier
	s_setprio 1
	v_mfma_f32_16x16x128_f8f6f4 v[132:135], v[136:143], v[68:75], v[132:135]
	v_mfma_f32_16x16x128_f8f6f4 v[124:127], v[156:163], v[68:75], v[124:127]
	v_mfma_f32_16x16x128_f8f6f4 v[116:119], v[136:143], v[194:201], v[116:119]
	v_mfma_f32_16x16x128_f8f6f4 v[108:111], v[156:163], v[194:201], v[108:111]
	v_mfma_f32_16x16x128_f8f6f4 v[100:103], v[136:143], v[228:235], v[144:147]
	v_mfma_f32_16x16x128_f8f6f4 v[92:95], v[156:163], v[228:235], v[180:183]
	v_mfma_f32_16x16x128_f8f6f4 v[84:87], v[136:143], v[236:243], v[186:189]
	v_mfma_f32_16x16x128_f8f6f4 v[76:79], v[156:163], v[236:243], v[190:193]
	s_setprio 0
	s_setprio 1
	v_mfma_f32_16x16x128_f8f6f4 v[128:131], v[164:171], v[68:75], v[128:131]
	v_mfma_f32_16x16x128_f8f6f4 v[120:123], v[172:179], v[68:75], v[120:123]
	v_mfma_f32_16x16x128_f8f6f4 v[112:115], v[164:171], v[194:201], v[112:115]
	v_mfma_f32_16x16x128_f8f6f4 v[104:107], v[172:179], v[194:201], v[104:107]
	v_mfma_f32_16x16x128_f8f6f4 v[96:99], v[164:171], v[228:235], v[202:205]
	v_mfma_f32_16x16x128_f8f6f4 v[88:91], v[172:179], v[228:235], v[206:209]
	v_mfma_f32_16x16x128_f8f6f4 v[80:83], v[164:171], v[236:243], v[210:213]
	v_mfma_f32_16x16x128_f8f6f4 v[72:75], v[172:179], v[236:243], v[214:217]
	s_setprio 0
	s_barrier
	v_mov_b32_e32 v184, v152
	ds_read_b128 v[194:197], v148 offset:49152
	ds_read_b128 v[228:231], v148 offset:51200
	ds_read_b128 v[198:201], v149 offset:49152
	ds_read_b128 v[232:235], v149 offset:51200
	ds_read_b128 v[236:239], v148 offset:53248
	ds_read_b128 v[244:247], v148 offset:55296
	ds_read_b128 v[240:243], v149 offset:53248
	ds_read_b128 v[248:251], v149 offset:55296
	s_mov_b32 m0, s57
	v_lshl_add_u64 v[60:61], s[36:37], 0, v[184:185]
	v_lshl_add_u64 v[60:61], v[60:61], 0, s[46:47]
	v_mov_b32_e32 v184, v153
	global_load_lds_dwordx4 v[60:61], off
	s_mov_b32 m0, s59
	v_lshl_add_u64 v[60:61], s[36:37], 0, v[184:185]
	v_lshl_add_u64 v[60:61], v[60:61], 0, s[46:47]
	global_load_lds_dwordx4 v[60:61], off
	s_add_u32 s36, s36, 0x20080
	v_mov_b32_e32 v60, v152
	s_addc_u32 s37, s37, 0
	s_mov_b32 m0, s66
	s_nop 0
	global_load_lds_dwordx4 v60, s[36:37]
	v_mov_b32_e32 v60, v153
	s_mov_b32 m0, s67
	s_nop 0
	global_load_lds_dwordx4 v60, s[36:37]
	v_mbcnt_lo_u32_b32 v60, -1, 0
	v_mbcnt_hi_u32_b32 v60, -1, v60
	s_mov_b32 s36, s61
	v_lshlrev_b32_e32 v60, 3, v60
	s_mov_b32 m0, s64
	v_lshl_or_b32 v60, s36, 9, v60
	v_add_u32_e32 v60, s78, v60
	ds_read_b32 v62, v60
	s_waitcnt lgkmcnt(0)
	v_lshlrev_b32_e32 v60, 10, v62
	v_and_or_b32 v184, v60, s69, v154
	s_nop 0
	v_lshl_add_u64 v[60:61], s[28:29], 0, v[184:185]
	v_lshl_add_u64 v[60:61], v[60:61], 0, s[46:47]
	global_load_lds_dwordx4 v[60:61], off
	v_bfe_u32 v60, v62, 16, 16
	v_lshl_or_b32 v184, v60, 10, v154
	s_mov_b32 m0, s65
	v_lshl_add_u64 v[60:61], s[28:29], 0, v[184:185]
	v_lshl_add_u64 v[60:61], v[60:61], 0, s[46:47]
	global_load_lds_dwordx4 v[60:61], off
	s_waitcnt vmcnt(8)
	s_waitcnt lgkmcnt(0)
	s_barrier
	s_setprio 1
	v_mfma_f32_16x16x128_f8f6f4 v[68:71], v[136:143], v[194:201], v[40:43]
	v_mfma_f32_16x16x128_f8f6f4 v[60:63], v[156:163], v[194:201], v[52:55]
	v_mfma_f32_16x16x128_f8f6f4 v[48:51], v[136:143], v[228:235], v[48:51]
	v_mfma_f32_16x16x128_f8f6f4 v[36:39], v[156:163], v[228:235], v[36:39]
	v_mfma_f32_16x16x128_f8f6f4 v[28:31], v[136:143], v[236:243], v[28:31]
	v_mfma_f32_16x16x128_f8f6f4 v[20:23], v[156:163], v[236:243], v[20:23]
	v_mfma_f32_16x16x128_f8f6f4 v[12:15], v[136:143], v[244:251], v[12:15]
	v_mfma_f32_16x16x128_f8f6f4 v[4:7], v[156:163], v[244:251], v[4:7]
	s_setprio 0
	s_setprio 1
	v_mfma_f32_16x16x128_f8f6f4 v[64:67], v[164:171], v[194:201], v[64:67]
	v_mfma_f32_16x16x128_f8f6f4 v[56:59], v[172:179], v[194:201], v[56:59]
	v_mfma_f32_16x16x128_f8f6f4 v[44:47], v[164:171], v[228:235], v[44:47]
	v_mfma_f32_16x16x128_f8f6f4 v[32:35], v[172:179], v[228:235], v[32:35]
	v_mfma_f32_16x16x128_f8f6f4 v[24:27], v[164:171], v[236:243], v[24:27]
	v_mfma_f32_16x16x128_f8f6f4 v[16:19], v[172:179], v[236:243], v[16:19]
	v_mfma_f32_16x16x128_f8f6f4 v[8:11], v[164:171], v[244:251], v[8:11]
	v_mfma_f32_16x16x128_f8f6f4 v[0:3], v[172:179], v[244:251], v[0:3]
	s_setprio 0
	s_barrier
	s_add_i32 s77, s77, 2
	s_add_u32 s24, s24, 0x100
	s_addc_u32 s25, s25, 0
	s_add_u32 s19, s19, 0x100
	s_addc_u32 s76, s76, 0
	.p2align	6

.LBB0_1113:
	s_ashr_i32 s25, s24, 31
	s_lshl_b64 s[22:23], s[24:25], 18
	s_add_u32 s22, s38, s22
	s_addc_u32 s23, s39, s23
	s_and_b64 s[34:35], s[10:11], exec
	s_cselect_b32 s7, s23, s29
	s_cselect_b32 s21, s22, s28
	s_add_u32 s28, s28, 0x20080
	s_addc_u32 s29, s29, 0
	s_add_u32 s25, s30, 0x100
	s_addc_u32 s80, s31, 0
	s_mov_b32 s81, -2
	ds_read_b128 v[128:131], v148
	ds_read_b128 v[136:139], v148 offset:2048
	ds_read_b128 v[132:135], v149
	ds_read_b128 v[140:143], v149 offset:2048
	ds_read_b128 v[152:155], v148 offset:16384
	ds_read_b128 v[160:163], v148 offset:18432
	ds_read_b128 v[156:159], v149 offset:16384
	ds_read_b128 v[164:167], v149 offset:18432
	s_add_u32 s30, s28, 0xfffe0080
	s_addc_u32 s31, s29, -1
	s_cmp_eq_u32 s81, 4
	s_cselect_b32 s31, s7, s31
	s_cselect_b32 s30, s21, s30
	s_cselect_b32 s35, s19, s80
	s_cselect_b32 s34, s18, s25
	v_mov_b32_e32 v144, v150
	ds_read_b128 v[168:171], v146
	ds_read_b128 v[176:179], v146 offset:2048
	ds_read_b128 v[172:175], v147
	ds_read_b128 v[180:183], v147 offset:2048
	ds_read_b128 v[194:197], v146 offset:4096
	ds_read_b128 v[228:231], v146 offset:6144
	ds_read_b128 v[198:201], v147 offset:4096
	ds_read_b128 v[232:235], v147 offset:6144
	s_add_i32 m0, s27, 0xc000
	s_nop 0
	global_load_lds_dwordx4 v144, s[28:29]
	v_mov_b32_e32 v144, v151
	s_add_i32 m0, s27, 0xe000
	s_nop 0
	global_load_lds_dwordx4 v144, s[28:29]
	s_waitcnt vmcnt(8)
	s_waitcnt lgkmcnt(0)
	s_barrier
	s_setprio 1
	s_waitcnt lgkmcnt(0)
	v_mfma_f32_16x16x128_f8f6f4 v[124:127], v[128:135], v[168:175], 0
	v_mfma_f32_16x16x128_f8f6f4 v[120:123], v[136:143], v[168:175], 0
	v_mfma_f32_16x16x128_f8f6f4 v[108:111], v[128:135], v[176:183], 0
	v_mfma_f32_16x16x128_f8f6f4 v[104:107], v[136:143], v[176:183], 0
	v_mfma_f32_16x16x128_f8f6f4 v[186:189], v[128:135], v[194:201], 0
	v_mfma_f32_16x16x128_f8f6f4 v[190:193], v[136:143], v[194:201], 0
	v_mfma_f32_16x16x128_f8f6f4 v[202:205], v[128:135], v[228:235], 0
	v_mfma_f32_16x16x128_f8f6f4 v[206:209], v[136:143], v[228:235], 0
	s_setprio 0
	s_setprio 1
	v_mfma_f32_16x16x128_f8f6f4 v[116:119], v[152:159], v[168:175], 0
	v_mfma_f32_16x16x128_f8f6f4 v[112:115], v[160:167], v[168:175], 0
	v_mfma_f32_16x16x128_f8f6f4 v[100:103], v[152:159], v[176:183], 0
	v_mfma_f32_16x16x128_f8f6f4 v[96:99], v[160:167], v[176:183], 0
	v_mfma_f32_16x16x128_f8f6f4 v[168:171], v[152:159], v[194:201], 0
	v_mfma_f32_16x16x128_f8f6f4 v[172:175], v[160:167], v[194:201], 0
	v_mfma_f32_16x16x128_f8f6f4 v[176:179], v[152:159], v[228:235], 0
	v_mfma_f32_16x16x128_f8f6f4 v[180:183], v[160:167], v[228:235], 0
	s_setprio 0
	s_barrier
	v_mov_b32_e32 v144, v150
	s_mov_b32 m0, s43
	s_nop 2
	ds_read_b128 v[64:67], v146 offset:16384
	ds_read_b128 v[72:75], v146 offset:18432
	ds_read_b128 v[68:71], v147 offset:16384
	ds_read_b128 v[76:79], v147 offset:18432
	ds_read_b128 v[80:83], v146 offset:20480
	ds_read_b128 v[88:91], v146 offset:22528
	ds_read_b128 v[84:87], v147 offset:20480
	ds_read_b128 v[92:95], v147 offset:22528
	s_add_u32 s82, s34, 0x20000
	global_load_lds_dwordx4 v144, s[34:35]
	v_mov_b32_e32 v144, v151
	s_mov_b32 m0, s44
	s_addc_u32 s83, s35, 0
	global_load_lds_dwordx4 v144, s[34:35]
	v_mov_b32_e32 v144, v150
	s_mov_b32 m0, s49
	s_nop 0
	global_load_lds_dwordx4 v144, s[82:83]
	v_mov_b32_e32 v144, v151
	s_mov_b32 m0, s50
	s_nop 0
	global_load_lds_dwordx4 v144, s[82:83]
	v_mov_b32_e32 v144, v150
	s_mov_b32 m0, s27
	s_nop 0
	global_load_lds_dwordx4 v144, s[30:31]
	v_mov_b32_e32 v144, v151
	s_mov_b32 m0, s51
	s_nop 0
	global_load_lds_dwordx4 v144, s[30:31]
	s_waitcnt vmcnt(8)
	s_waitcnt lgkmcnt(0)
	s_barrier
	s_setprio 1
	s_waitcnt lgkmcnt(0)
	v_mfma_f32_16x16x128_f8f6f4 v[60:63], v[128:135], v[64:71], 0
	v_mfma_f32_16x16x128_f8f6f4 v[56:59], v[136:143], v[64:71], 0
	v_mfma_f32_16x16x128_f8f6f4 v[194:197], v[128:135], v[72:79], 0
	v_mfma_f32_16x16x128_f8f6f4 v[198:201], v[136:143], v[72:79], 0
	v_mfma_f32_16x16x128_f8f6f4 v[210:213], v[128:135], v[80:87], 0
	v_mfma_f32_16x16x128_f8f6f4 v[214:217], v[136:143], v[80:87], 0
	v_mfma_f32_16x16x128_f8f6f4 v[218:221], v[128:135], v[88:95], 0
	v_mfma_f32_16x16x128_f8f6f4 v[222:225], v[136:143], v[88:95], 0
	s_setprio 0
	s_setprio 1
	v_mfma_f32_16x16x128_f8f6f4 v[52:55], v[152:159], v[64:71], 0
	v_mfma_f32_16x16x128_f8f6f4 v[48:51], v[160:167], v[64:71], 0
	v_mfma_f32_16x16x128_f8f6f4 v[228:231], v[152:159], v[72:79], 0
	v_mfma_f32_16x16x128_f8f6f4 v[232:235], v[160:167], v[72:79], 0
	v_mfma_f32_16x16x128_f8f6f4 v[236:239], v[152:159], v[80:87], 0
	v_mfma_f32_16x16x128_f8f6f4 v[240:243], v[160:167], v[80:87], 0
	v_mfma_f32_16x16x128_f8f6f4 v[244:247], v[152:159], v[88:95], 0
	v_mfma_f32_16x16x128_f8f6f4 v[248:251], v[160:167], v[88:95], 0
	s_setprio 0
	s_barrier
	s_nop 4
	ds_read_b128 v[0:3], v148 offset:32768
	ds_read_b128 v[16:19], v148 offset:34816
	ds_read_b128 v[4:7], v149 offset:32768
	ds_read_b128 v[20:23], v149 offset:34816
	ds_read_b128 v[128:131], v148 offset:49152
	ds_read_b128 v[136:139], v148 offset:51200
	ds_read_b128 v[132:135], v149 offset:49152
	ds_read_b128 v[140:143], v149 offset:51200
	s_add_u32 s82, s30, 0x20000
	v_mov_b32_e32 v64, v150
	s_mov_b32 m0, s54
	ds_read_b128 v[8:11], v146 offset:32768
	ds_read_b128 v[24:27], v146 offset:34816
	ds_read_b128 v[12:15], v147 offset:32768
	ds_read_b128 v[28:31], v147 offset:34816
	ds_read_b128 v[32:35], v146 offset:36864
	ds_read_b128 v[40:43], v146 offset:38912
	ds_read_b128 v[36:39], v147 offset:36864
	ds_read_b128 v[44:47], v147 offset:38912
	s_addc_u32 s83, s31, 0
	s_nop 0
	global_load_lds_dwordx4 v64, s[82:83]
	v_mov_b32_e32 v64, v151
	s_mov_b32 m0, s55
	s_nop 0
	global_load_lds_dwordx4 v64, s[82:83]
	s_waitcnt vmcnt(8)
	s_waitcnt lgkmcnt(0)
	s_barrier
	s_setprio 1
	s_waitcnt lgkmcnt(0)
	v_mfma_f32_16x16x128_f8f6f4 v[124:127], v[0:7], v[8:15], v[124:127]
	v_mfma_f32_16x16x128_f8f6f4 v[120:123], v[16:23], v[8:15], v[120:123]
	v_mfma_f32_16x16x128_f8f6f4 v[108:111], v[0:7], v[24:31], v[108:111]
	v_mfma_f32_16x16x128_f8f6f4 v[104:107], v[16:23], v[24:31], v[104:107]
	v_mfma_f32_16x16x128_f8f6f4 v[92:95], v[0:7], v[32:39], v[186:189]
	v_mfma_f32_16x16x128_f8f6f4 v[88:91], v[16:23], v[32:39], v[190:193]
	v_mfma_f32_16x16x128_f8f6f4 v[76:79], v[0:7], v[40:47], v[202:205]
	v_mfma_f32_16x16x128_f8f6f4 v[72:75], v[16:23], v[40:47], v[206:209]
	s_setprio 0
	s_setprio 1
	v_mfma_f32_16x16x128_f8f6f4 v[116:119], v[128:135], v[8:15], v[116:119]
	v_mfma_f32_16x16x128_f8f6f4 v[112:115], v[136:143], v[8:15], v[112:115]
	v_mfma_f32_16x16x128_f8f6f4 v[100:103], v[128:135], v[24:31], v[100:103]
	v_mfma_f32_16x16x128_f8f6f4 v[96:99], v[136:143], v[24:31], v[96:99]
	v_mfma_f32_16x16x128_f8f6f4 v[84:87], v[128:135], v[32:39], v[168:171]
	v_mfma_f32_16x16x128_f8f6f4 v[80:83], v[136:143], v[32:39], v[172:175]
	v_mfma_f32_16x16x128_f8f6f4 v[68:71], v[128:135], v[40:47], v[176:179]
	v_mfma_f32_16x16x128_f8f6f4 v[64:67], v[136:143], v[40:47], v[180:183]
	s_setprio 0
	s_barrier
	v_mov_b32_e32 v184, v150
	ds_read_b128 v[32:35], v146 offset:49152
	ds_read_b128 v[152:155], v146 offset:51200
	ds_read_b128 v[36:39], v147 offset:49152
	ds_read_b128 v[156:159], v147 offset:51200
	ds_read_b128 v[160:163], v146 offset:53248
	ds_read_b128 v[168:171], v146 offset:55296
	ds_read_b128 v[164:167], v147 offset:53248
	ds_read_b128 v[172:175], v147 offset:55296
	s_mov_b32 m0, s56
	v_lshl_add_u64 v[8:9], s[34:35], 0, v[184:185]
	v_lshl_add_u64 v[8:9], v[8:9], 0, s[46:47]
	v_mov_b32_e32 v184, v151
	global_load_lds_dwordx4 v[8:9], off
	s_mov_b32 m0, s57
	v_lshl_add_u64 v[8:9], s[34:35], 0, v[184:185]
	v_lshl_add_u64 v[8:9], v[8:9], 0, s[46:47]
	global_load_lds_dwordx4 v[8:9], off
	s_add_u32 s34, s34, 0x20080
	v_mov_b32_e32 v8, v150
	s_addc_u32 s35, s35, 0
	s_mov_b32 m0, s65
	v_mov_b32_e32 v184, v150
	global_load_lds_dwordx4 v8, s[34:35]
	v_mov_b32_e32 v8, v151
	s_mov_b32 m0, s66
	s_nop 0
	global_load_lds_dwordx4 v8, s[34:35]
	s_mov_b32 m0, s59
	v_lshl_add_u64 v[8:9], s[30:31], 0, v[184:185]
	v_lshl_add_u64 v[8:9], v[8:9], 0, s[46:47]
	v_mov_b32_e32 v184, v151
	global_load_lds_dwordx4 v[8:9], off
	s_mov_b32 m0, s64
	v_lshl_add_u64 v[8:9], s[30:31], 0, v[184:185]
	v_lshl_add_u64 v[8:9], v[8:9], 0, s[46:47]
	global_load_lds_dwordx4 v[8:9], off
	s_waitcnt vmcnt(8)
	s_waitcnt lgkmcnt(0)
	s_barrier
	s_setprio 1
	s_waitcnt lgkmcnt(0)
	v_mfma_f32_16x16x128_f8f6f4 v[60:63], v[0:7], v[32:39], v[60:63]
	v_mfma_f32_16x16x128_f8f6f4 v[56:59], v[16:23], v[32:39], v[56:59]
	v_mfma_f32_16x16x128_f8f6f4 v[44:47], v[0:7], v[152:159], v[194:197]
	v_mfma_f32_16x16x128_f8f6f4 v[40:43], v[16:23], v[152:159], v[198:201]
	v_mfma_f32_16x16x128_f8f6f4 v[28:31], v[0:7], v[160:167], v[210:213]
	v_mfma_f32_16x16x128_f8f6f4 v[24:27], v[16:23], v[160:167], v[214:217]
	v_mfma_f32_16x16x128_f8f6f4 v[12:15], v[0:7], v[168:175], v[218:221]
	v_mfma_f32_16x16x128_f8f6f4 v[8:11], v[16:23], v[168:175], v[222:225]
	s_setprio 0
	s_setprio 1
	v_mfma_f32_16x16x128_f8f6f4 v[52:55], v[128:135], v[32:39], v[52:55]
	v_mfma_f32_16x16x128_f8f6f4 v[48:51], v[136:143], v[32:39], v[48:51]
	v_mfma_f32_16x16x128_f8f6f4 v[36:39], v[128:135], v[152:159], v[228:231]
	v_mfma_f32_16x16x128_f8f6f4 v[32:35], v[136:143], v[152:159], v[232:235]
	v_mfma_f32_16x16x128_f8f6f4 v[20:23], v[128:135], v[160:167], v[236:239]
	v_mfma_f32_16x16x128_f8f6f4 v[16:19], v[136:143], v[160:167], v[240:243]
	v_mfma_f32_16x16x128_f8f6f4 v[4:7], v[128:135], v[168:175], v[244:247]
	v_mfma_f32_16x16x128_f8f6f4 v[0:3], v[136:143], v[168:175], v[248:251]
	s_setprio 0
	s_barrier
	s_add_i32 s81, s81, 2
	s_add_u32 s28, s28, 0x100
	s_addc_u32 s29, s29, 0
	s_add_u32 s25, s25, 0x100
	s_addc_u32 s80, s80, 0
	.p2align	6
